# per-half A/B of the static priority raise: s_setprio 1 for waves 0-3 during attention and top-k phases, on top of v062
# baseline (speedup 1.0000x reference)
.LBB0_333:
	s_cmp_ge_u32 s89, 4
	s_cbranch_scc1 .Laprio_4
	s_setprio 1
